# gemm_in: lean epilogue (convert + 16 row stores, one base address + constant offsets) for column tiles without attention values; original epilogue kept for the V tiles
# speedup vs baseline: 1.0005x; 1.0005x over previous
; __device__ __forceinline__ unsigned cvt_pk_bf16(float lo, float hi) { f32x2c v = {lo, hi}; bf16x2c b = __builtin_convertvector(v, bf16x2c); return __builtin_bit_cast(unsigned, b); }
;     __device__ __forceinline__ void operator()(const f32x4 (&acc)[2][2][4][2], const Unit& u, int wr, int wc, int fr, int fq) const {
;         const int row0 = u.row0 + wr * 64 + fr, col0 = u.pn * BM + wc * 32 + 8 * fq;
; #pragma unroll
;         for (int ai = 0; ai < 2; ++ai)
; #pragma unroll
;             for (int m = 0; m < 4; ++m) { const int row = row0 + ai * HALF + m * 16; bf16_t* rowp = O + (size_t)row * INW + col0;
;                 const int b = row / LT, t = row - b * LT; const int tp = (t & ~12) | ((t & 4) << 1) | ((t & 8) >> 1);
; #pragma unroll
;                 for (int bj = 0; bj < 2; ++bj) { const f32x4 v0 = acc[ai][bj][m][0], v1 = acc[ai][bj][m][1];
;                     u32x4 w; w.x = cvt_pk_bf16(v0[0], v0[1]); w.y = cvt_pk_bf16(v0[2], v0[3]); w.z = cvt_pk_bf16(v1[0], v1[1]); w.w = cvt_pk_bf16(v1[2], v1[3]);
;                     *(u32x4*)(rowp + bj * HALF) = w;
.LBB0_130:
	s_cmp_eq_u32 s16, 4
	s_cbranch_scc1 .Lepi_full
	s_cmp_eq_u32 s16, 1
	s_cbranch_scc1 .Lepi_full
	v_add_u32_e32 v137, s57, v190
	s_lshl_b32 s0, s16, 8
	s_or_b32 s25, s0, s51
	v_mov_b64_e32 v[132:133], s[18:19]
	v_or_b32_e32 v130, s25, v191
	v_mad_i64_i32 v[132:133], s[4:5], v137, s97, v[132:133]
	v_ashrrev_i32_e32 v131, 31, v130
	v_lshl_add_u64 v[134:135], v[130:131], 1, v[132:133]
	v_cvt_pk_bf16_f32 v140, v126, v127
	v_cvt_pk_bf16_f32 v141, v128, v129
	v_cvt_pk_bf16_f32 v142, v122, v123
	v_cvt_pk_bf16_f32 v143, v124, v125
	global_store_dwordx4 v[134:135], v[140:143], off
	v_cvt_pk_bf16_f32 v144, v110, v111
	v_cvt_pk_bf16_f32 v145, v112, v113
	v_cvt_pk_bf16_f32 v146, v106, v107
	v_cvt_pk_bf16_f32 v147, v108, v109
	global_store_dwordx4 v[134:135], v[144:147], off offset:256
	s_mov_b32 s0, 0x16000
	s_mov_b32 s1, 0
	v_lshl_add_u64 v[138:139], v[134:135], 0, s[0:1]
	v_cvt_pk_bf16_f32 v140, v118, v119
	v_cvt_pk_bf16_f32 v141, v120, v121
	v_cvt_pk_bf16_f32 v142, v114, v115
	v_cvt_pk_bf16_f32 v143, v116, v117
	global_store_dwordx4 v[138:139], v[140:143], off
	v_cvt_pk_bf16_f32 v144, v94, v95
	v_cvt_pk_bf16_f32 v145, v96, v97
	v_cvt_pk_bf16_f32 v146, v90, v91
	v_cvt_pk_bf16_f32 v147, v92, v93
	global_store_dwordx4 v[138:139], v[144:147], off offset:256
	s_mov_b32 s0, 0x2c000
	s_mov_b32 s1, 0
	v_lshl_add_u64 v[138:139], v[134:135], 0, s[0:1]
	v_cvt_pk_bf16_f32 v140, v102, v103
	v_cvt_pk_bf16_f32 v141, v104, v105
	v_cvt_pk_bf16_f32 v142, v98, v99
	v_cvt_pk_bf16_f32 v143, v100, v101
	global_store_dwordx4 v[138:139], v[140:143], off
	v_cvt_pk_bf16_f32 v144, v78, v79
	v_cvt_pk_bf16_f32 v145, v80, v81
	v_cvt_pk_bf16_f32 v146, v74, v75
	v_cvt_pk_bf16_f32 v147, v76, v77
	global_store_dwordx4 v[138:139], v[144:147], off offset:256
	s_mov_b32 s0, 0x42000
	s_mov_b32 s1, 0
	v_lshl_add_u64 v[138:139], v[134:135], 0, s[0:1]
	v_cvt_pk_bf16_f32 v140, v86, v87
	v_cvt_pk_bf16_f32 v141, v88, v89
	v_cvt_pk_bf16_f32 v142, v82, v83
	v_cvt_pk_bf16_f32 v143, v84, v85
	global_store_dwordx4 v[138:139], v[140:143], off
	v_cvt_pk_bf16_f32 v144, v70, v71
	v_cvt_pk_bf16_f32 v145, v72, v73
	v_cvt_pk_bf16_f32 v146, v66, v67
	v_cvt_pk_bf16_f32 v147, v68, v69
	global_store_dwordx4 v[138:139], v[144:147], off offset:256
	s_mov_b32 s0, 0xb0000
	s_mov_b32 s1, 0
	v_lshl_add_u64 v[138:139], v[134:135], 0, s[0:1]
	v_cvt_pk_bf16_f32 v140, v62, v63
	v_cvt_pk_bf16_f32 v141, v64, v65
	v_cvt_pk_bf16_f32 v142, v58, v59
	v_cvt_pk_bf16_f32 v143, v60, v61
	global_store_dwordx4 v[138:139], v[140:143], off
	v_cvt_pk_bf16_f32 v144, v54, v55
	v_cvt_pk_bf16_f32 v145, v56, v57
	v_cvt_pk_bf16_f32 v146, v50, v51
	v_cvt_pk_bf16_f32 v147, v52, v53
	global_store_dwordx4 v[138:139], v[144:147], off offset:256
	s_mov_b32 s0, 0xc6000
	s_mov_b32 s1, 0
	v_lshl_add_u64 v[138:139], v[134:135], 0, s[0:1]
	v_cvt_pk_bf16_f32 v140, v46, v47
	v_cvt_pk_bf16_f32 v141, v48, v49
	v_cvt_pk_bf16_f32 v142, v42, v43
	v_cvt_pk_bf16_f32 v143, v44, v45
	global_store_dwordx4 v[138:139], v[140:143], off
	v_cvt_pk_bf16_f32 v144, v38, v39
	v_cvt_pk_bf16_f32 v145, v40, v41
	v_cvt_pk_bf16_f32 v146, v34, v35
	v_cvt_pk_bf16_f32 v147, v36, v37
	global_store_dwordx4 v[138:139], v[144:147], off offset:256
	s_mov_b32 s0, 0xdc000
	s_mov_b32 s1, 0
	v_lshl_add_u64 v[138:139], v[134:135], 0, s[0:1]
	v_cvt_pk_bf16_f32 v140, v30, v31
	v_cvt_pk_bf16_f32 v141, v32, v33
	v_cvt_pk_bf16_f32 v142, v26, v27
	v_cvt_pk_bf16_f32 v143, v28, v29
	global_store_dwordx4 v[138:139], v[140:143], off
	v_cvt_pk_bf16_f32 v144, v22, v23
	v_cvt_pk_bf16_f32 v145, v24, v25
	v_cvt_pk_bf16_f32 v146, v18, v19
	v_cvt_pk_bf16_f32 v147, v20, v21
	global_store_dwordx4 v[138:139], v[144:147], off offset:256
	s_mov_b32 s0, 0xf2000
	s_mov_b32 s1, 0
	v_lshl_add_u64 v[138:139], v[134:135], 0, s[0:1]
	v_cvt_pk_bf16_f32 v140, v14, v15
	v_cvt_pk_bf16_f32 v141, v16, v17
	v_cvt_pk_bf16_f32 v142, v10, v11
	v_cvt_pk_bf16_f32 v143, v12, v13
	global_store_dwordx4 v[138:139], v[140:143], off
	v_cvt_pk_bf16_f32 v144, v6, v7
	v_cvt_pk_bf16_f32 v145, v8, v9
	v_cvt_pk_bf16_f32 v146, v2, v3
	v_cvt_pk_bf16_f32 v147, v4, v5
	global_store_dwordx4 v[138:139], v[144:147], off offset:256
	s_mov_b64 s[28:29], exec
	s_branch .LBB0_117
